# v3 + moe_tables counter loads batched + ml_c loop-top vmcnt(12)
# speedup vs baseline: 1.0288x; 1.0053x over previous
.LBB0_1072:
	v_readlane_b32 s0, v247, 0
	s_cmp_lt_u32 s0, 64
	s_cselect_b64 s[30:31], -1, 0
	v_lshlrev_b32_e32 v38, 2, v164
	s_add_i32 s14, 0, 0x19600
	s_add_i32 s22, 0, 0x19700
	s_add_i32 s23, 0, 0x19800
	v_or_b32_e32 v42, 0xa00, v0
	v_add_u32_e32 v102, s14, v38
	v_add_u32_e32 v103, s22, v38
	v_add_u32_e32 v104, s23, v38
	v_and_b32_e32 v38, 0x78, v155
	v_lshrrev_b32_e32 v115, 7, v42
	v_or_b32_e32 v42, 0xe00, v0
	v_lshlrev_b32_e32 v78, 1, v38
	v_lshrrev_b32_e32 v118, 7, v42
	v_or_b32_e32 v42, 0x1200, v0
	v_add_u32_e32 v39, 0, v78
	v_mul_u32_u24_e32 v38, 0x88, v218
	v_lshrrev_b32_e32 v121, 7, v42
	v_or_b32_e32 v42, 0x1600, v0
	v_lshl_add_u32 v105, v38, 1, v39
	v_mul_u32_u24_e32 v38, 0x88, v85
	v_lshrrev_b32_e32 v124, 7, v42
	v_or_b32_e32 v42, 0x1a00, v0
	v_lshl_add_u32 v106, v38, 1, v39
	v_and_b32_e32 v38, 0x7f, v0
	s_movk_i32 s25, 0x90
	v_or_b32_e32 v43, 0x600, v0
	v_or_b32_e32 v41, 0x800, v0
	v_lshrrev_b32_e32 v127, 7, v42
	v_or_b32_e32 v42, 0x1e00, v0
	v_mad_u32_u24 v40, v38, s25, 0
	v_lshrrev_b32_e32 v107, 7, v0
	v_lshrrev_b32_e32 v111, 7, v43
	v_lshrrev_b32_e32 v113, 7, v41
	v_lshrrev_b32_e32 v130, 7, v42
	v_lshl_add_u32 v108, v107, 1, v40
	v_lshl_add_u32 v109, v100, 1, v40
	v_lshl_add_u32 v110, v101, 1, v40
	v_lshl_add_u32 v112, v111, 1, v40
	v_lshl_add_u32 v114, v113, 1, v40
	v_lshl_add_u32 v116, v115, 1, v40
	v_lshl_add_u32 v119, v118, 1, v40
	v_lshl_add_u32 v122, v121, 1, v40
	v_lshl_add_u32 v125, v124, 1, v40
	v_lshl_add_u32 v128, v127, 1, v40
	v_lshl_add_u32 v131, v130, 1, v40
	v_lshrrev_b32_e32 v40, 4, v1
	v_lshlrev_b32_e32 v1, 3, v1
	v_and_b32_e32 v44, 0x3f80, v1
	v_lshlrev_b32_e32 v1, 3, v43
	v_and_b32_e32 v46, 0x3f80, v1
	s_movk_i32 s20, 0x9f0
	v_mov_b32_e32 v1, 0x800
	s_movk_i32 s53, 0x800
	s_movk_i32 s16, 0x100
	v_bitop3_b32 v1, v0, s20, v1 bitop3:0xc8
	v_cmp_gt_u32_e64 s[16:17], s16, v0
	s_add_u32 s34, s26, 0x3b500000
	v_cmp_eq_u32_e32 vcc, s53, v1
	s_addc_u32 s35, s27, 0
	s_and_b64 s[36:37], s[16:17], vcc
	s_add_u32 s54, s26, 0x50600008
	s_addc_u32 s55, s27, 0
	s_add_u32 s38, s26, 0x50500000
	s_addc_u32 s39, s27, 0
	s_and_b64 s[20:21], s[92:93], exec
	s_cselect_b32 s44, 0, 5
	s_mul_i32 s20, s43, 0x900
	v_mul_u32_u24_e32 v48, 0x110, v40
	v_lshrrev_b32_e32 v40, 4, v43
	s_add_i32 s20, s20, 0
	s_lshl_b32 s47, s43, 6
	s_mul_i32 s57, s44, 0x1100
	v_mul_u32_u24_e32 v49, 0x110, v40
	v_lshrrev_b32_e32 v40, 4, v41
	v_mov_b32_e32 v79, 0
	v_lshrrev_b32_e32 v1, 2, v0
	s_add_i32 s45, s20, 0x17200
	s_add_i32 s46, s52, 0
	s_add_i32 s48, s22, s47
	s_add_i32 s58, s57, 0x1100
	v_mul_u32_u24_e32 v50, 0x110, v40
	v_lshl_add_u64 v[40:41], s[26:27], 0, v[78:79]
	s_mov_b64 s[18:19], 0x55000000
	v_and_b32_e32 v84, 15, v0
	v_and_b32_e32 v132, 12, v1
	s_cmp_eq_u32 s44, 5
	v_lshl_add_u64 v[82:83], v[40:41], 0, s[18:19]
	v_mul_u32_u24_e32 v41, 0x110, v84
	v_and_b32_e32 v43, 48, v0
	v_cmp_eq_u32_e32 vcc, 0, v84
	s_cselect_b64 s[20:21], -1, 0
	v_lshl_or_b32 v141, s43, 4, v132
	v_add3_u32 v133, 0, v41, v43
	s_and_b64 s[40:41], vcc, s[20:21]
	s_add_i32 s20, 0, 0x19900
	v_add3_u32 v138, s46, v41, v43
	v_lshlrev_b32_e32 v41, 2, v141
	v_or_b32_e32 v145, 1, v141
	v_add_u32_e32 v142, s20, v41
	v_add_u32_e32 v143, s23, v41
	v_add_u32_e32 v144, s22, v41
	v_lshlrev_b32_e32 v41, 2, v145
	v_or_b32_e32 v149, 2, v141
	v_add_u32_e32 v146, s20, v41
	v_add_u32_e32 v147, s23, v41
	v_add_u32_e32 v148, s22, v41
	v_lshlrev_b32_e32 v41, 2, v149
	v_or_b32_e32 v153, 3, v141
	s_add_i32 s47, s47, s20
	v_add_u32_e32 v150, s20, v41
	v_add_u32_e32 v151, s23, v41
	v_add_u32_e32 v152, s22, v41
	v_lshlrev_b32_e32 v41, 2, v153
	s_add_u32 s59, s26, 0x5e100000
	v_add_u32_e32 v154, s20, v41
	v_add_u32_e32 v156, s23, v41
	v_add_u32_e32 v157, s22, v41
	v_bfe_u32 v41, v0, 4, 2
	s_movk_i32 s42, 0x110
	v_mul_u32_u24_e32 v45, 0x110, v218
	v_mul_u32_u24_e32 v47, 0x110, v85
	s_movk_i32 s14, 0x300
	v_lshlrev_b32_e32 v40, 7, v218
	v_lshlrev_b32_e32 v42, 7, v85
	s_movk_i32 s18, 0x210
	v_mul_u32_u24_e32 v51, 0x90, v84
	v_lshlrev_b32_e32 v52, 7, v84
	s_addc_u32 s60, s27, 0
	s_lshl_b32 s21, s44, 4
	v_lshlrev_b32_e32 v158, 4, v41
	v_mul_u32_u24_e32 v41, 0x240, v41
	v_cmp_lt_u32_e64 s[0:1], 15, v164
	v_cmp_lt_u32_e64 s[4:5], 31, v164
	v_cmp_lt_u32_e64 s[6:7], 47, v164
	v_cmp_gt_u32_e64 s[8:9], 16, v164
	v_cmp_gt_u32_e64 s[10:11], 32, v164
	v_cmp_gt_u32_e64 s[12:13], 48, v164
	s_mov_b32 s28, 0
	v_or_b32_e32 v117, 24, v107
	v_or_b32_e32 v120, 32, v107
	v_or_b32_e32 v123, 40, v107
	v_or_b32_e32 v126, 48, v107
	v_or_b32_e32 v129, 56, v107
	v_cmp_gt_u32_e64 s[14:15], s14, v0
	v_lshl_add_u64 v[80:81], s[34:35], 0, v[78:79]
	v_cmp_gt_u32_e64 s[18:19], s18, v0
	s_mul_i32 s56, s44, 0x900
	v_add_u32_e32 v134, s47, v164
	v_or_b32_e32 v1, 0x200, v0
	v_lshl_add_u32 v135, v164, 1, 0
	v_add3_u32 v136, s45, v51, v43
	v_sub_u32_e32 v137, v133, v52
	v_add_u32_e32 v139, 0xd900, v133
	v_lshl_add_u32 v140, v132, 2, s48
	v_mad_u32_u24 v159, v84, s42, v158
	v_lshl_or_b32 v160, v84, 1, v41
	v_mov_b32_e32 v161, 0xff61b1e6
	v_add_u32_e32 v162, v39, v45
	v_add_u32_e32 v163, v39, v47
	v_add_u32_e32 v168, v39, v48
	v_add_u32_e32 v169, v39, v49
	v_add_u32_e32 v170, v39, v50
	s_movk_i32 s61, 0x2e00
	v_lshlrev_b32_e32 v86, 1, v38
	v_lshlrev_b32_e32 v88, 1, v40
	v_lshlrev_b32_e32 v90, 1, v42
	v_lshlrev_b32_e32 v92, 1, v44
	v_lshlrev_b32_e32 v94, 1, v46
	s_mov_b32 s42, 0x3db504f3
	s_lshl_b32 s44, s21, 1
	v_mov_b32_e32 v171, 0x3f80
	v_mov_b32_e32 v173, 0x8100
	s_waitcnt vmcnt(0)
	s_branch .LBB0_1074

.LBB0_1074:
	s_mul_hi_i32 s20, s24, 0x38e38e39
	s_lshr_b32 s21, s20, 31
	s_ashr_i32 s45, s20, 3
	s_add_i32 s45, s45, s21
	s_and_b32 s62, s45, 1
	s_cmp_eq_u32 s62, 0
	s_cselect_b64 s[20:21], -1, 0
	s_cmp_eq_u32 s62, 1
	v_cndmask_b32_e64 v38, 0, 1, s[30:31]
	s_cselect_b64 s[46:47], -1, 0
	s_waitcnt vmcnt(12)
	v_mov_b32_e32 v78, v186
	v_cmp_ne_u32_e64 s[22:23], 1, v38
	s_andn2_b64 vcc, exec, s[30:31]
	s_cbranch_vccnz .LBB0_1080
	s_nop 0
	v_add_f32_dpp v38, v87, v87 row_shr:1 row_mask:0xf bank_mask:0xf bound_ctrl:1
	s_and_b64 vcc, exec, s[46:47]
	s_nop 0
	v_add_f32_dpp v38, v38, v38 row_shr:2 row_mask:0xf bank_mask:0xf bound_ctrl:1
	s_nop 1
	v_add_f32_dpp v38, v38, v38 row_shr:4 row_mask:0xf bank_mask:0xf bound_ctrl:1
	s_nop 1
	v_add_f32_dpp v38, v38, v38 row_shr:8 row_mask:0xf bank_mask:0xf bound_ctrl:1
	s_nop 0
	v_readlane_b32 s48, v38, 15
	v_readlane_b32 s49, v38, 31
	v_readlane_b32 s50, v38, 47
	v_mov_b32_e32 v39, s48
	v_cndmask_b32_e64 v39, 0, v39, s[0:1]
	v_add_f32_e32 v38, v38, v39
	v_mov_b32_e32 v39, s49
	v_cndmask_b32_e64 v39, 0, v39, s[4:5]
	v_add_f32_e32 v38, v38, v39
	v_mov_b32_e32 v39, s50
	v_cndmask_b32_e64 v39, 0, v39, s[6:7]
	v_add_f32_e32 v38, v38, v39
	s_nop 0
	v_readlane_b32 s48, v38, 63
	s_nop 1
	v_sub_f32_e32 v39, s48, v38
	v_add_f32_e32 v39, v87, v39
	v_cndmask_b32_e64 v38, v39, v38, s[20:21]
	v_sub_f32_e32 v39, v89, v38
	s_mov_b64 s[48:49], -1
	v_max_f32_e32 v40, v39, v39
	s_cbranch_vccz .LBB0_1077
	v_mov_b32_e32 v41, 0xff61b1e6
	v_mov_b32_e32 v42, 0xff61b1e6
	s_nop 0
	v_mov_b32_dpp v41, v39 row_shl:1 row_mask:0xf bank_mask:0xf
	v_max_f32_e32 v41, v41, v41
	v_max_f32_e32 v41, v40, v41
	s_nop 1
	v_mov_b32_dpp v42, v41 row_shl:2 row_mask:0xf bank_mask:0xf
	v_max_f32_e32 v42, v42, v42
	v_max_f32_e32 v41, v41, v42
	v_mov_b32_e32 v42, 0xff61b1e6
	s_nop 1
	v_mov_b32_dpp v42, v41 row_shl:4 row_mask:0xf bank_mask:0xf
	v_max_f32_e32 v42, v42, v42
	v_max_f32_e32 v41, v41, v42
	v_mov_b32_e32 v42, 0xff61b1e6
	s_nop 1
	v_mov_b32_dpp v42, v41 row_shl:8 row_mask:0xf bank_mask:0xf
	v_max_f32_e32 v42, v42, v42
	v_max_f32_e32 v41, v41, v42
	s_nop 0
	v_readlane_b32 s47, v41, 32
	v_readlane_b32 s48, v41, 48
	v_readlane_b32 s46, v41, 16
	v_max_f32_e64 v42, s47, s47
	v_max_f32_e64 v43, s48, s48
	v_mov_b32_e32 v44, s48
	v_max_f32_e32 v42, v43, v42
	v_max_f32_e64 v43, s46, s46
	v_cndmask_b32_e64 v44, v161, v44, s[12:13]
	v_max_f32_e32 v43, v42, v43
	v_cndmask_b32_e64 v42, v44, v42, s[10:11]
	v_cndmask_b32_e64 v42, v42, v43, s[8:9]
	v_max_f32_e32 v42, v42, v42
	v_max_f32_e32 v41, v41, v42
	s_mov_b64 s[48:49], 0

.LBB0_3224:
.LBB0_3225:
	s_mov_b32 s25, 1
	s_andn2_b64 vcc, exec, s[4:5]
	v_cmp_lt_u32_e64 s[0:1], 15, v164
	v_cmp_lt_u32_e64 s[4:5], 31, v164
	v_cmp_lt_u32_e64 s[6:7], 47, v164
	s_mul_i32 s56, s43, 0x1100
	s_cbranch_vccnz .LBB0_3280
	v_readlane_b32 s8, v247, 0
	s_cmp_lt_u32 s8, 64
	s_cselect_b64 s[28:29], -1, 0
	v_lshlrev_b32_e32 v38, 2, v164
	s_add_i32 s14, 0, 0x19600
	s_add_i32 s22, 0, 0x19700
	s_add_i32 s23, 0, 0x19800
	v_or_b32_e32 v42, 0xa00, v0
	v_add_u32_e32 v103, s14, v38
	v_add_u32_e32 v104, s22, v38
	v_add_u32_e32 v105, s23, v38
	v_and_b32_e32 v38, 0x78, v153
	v_lshrrev_b32_e32 v115, 7, v42
	v_or_b32_e32 v42, 0xe00, v0
	v_lshlrev_b32_e32 v78, 1, v38
	v_lshrrev_b32_e32 v118, 7, v42
	v_or_b32_e32 v42, 0x1200, v0
	v_add_u32_e32 v39, 0, v78
	v_mul_u32_u24_e32 v38, 0x88, v218
	v_lshrrev_b32_e32 v121, 7, v42
	v_or_b32_e32 v42, 0x1600, v0
	v_lshl_add_u32 v106, v38, 1, v39
	v_mul_u32_u24_e32 v38, 0x88, v85
	v_lshrrev_b32_e32 v124, 7, v42
	v_or_b32_e32 v42, 0x1a00, v0
	v_lshl_add_u32 v107, v38, 1, v39
	v_and_b32_e32 v38, 0x7f, v0
	s_movk_i32 s57, 0x90
	v_or_b32_e32 v43, 0x600, v0
	v_or_b32_e32 v41, 0x800, v0
	v_lshrrev_b32_e32 v127, 7, v42
	v_or_b32_e32 v42, 0x1e00, v0
	v_mad_u32_u24 v40, v38, s57, 0
	v_lshrrev_b32_e32 v111, 7, v43
	v_lshrrev_b32_e32 v113, 7, v41
	v_lshrrev_b32_e32 v130, 7, v42
	v_lshl_add_u32 v108, v100, 1, v40
	v_lshl_add_u32 v109, v101, 1, v40
	v_lshl_add_u32 v110, v102, 1, v40
	v_lshl_add_u32 v112, v111, 1, v40
	v_lshl_add_u32 v114, v113, 1, v40
	v_lshl_add_u32 v116, v115, 1, v40
	v_lshl_add_u32 v119, v118, 1, v40
	v_lshl_add_u32 v122, v121, 1, v40
	v_lshl_add_u32 v125, v124, 1, v40
	v_lshl_add_u32 v128, v127, 1, v40
	v_lshl_add_u32 v131, v130, 1, v40
	v_lshrrev_b32_e32 v40, 4, v1
	v_lshlrev_b32_e32 v1, 3, v1
	v_and_b32_e32 v44, 0x3f80, v1
	v_lshlrev_b32_e32 v1, 3, v43
	v_and_b32_e32 v46, 0x3f80, v1
	s_movk_i32 s20, 0x9f0
	v_mov_b32_e32 v1, 0x800
	s_movk_i32 s58, 0x800
	s_movk_i32 s16, 0x100
	v_bitop3_b32 v1, v0, s20, v1 bitop3:0xc8
	v_cmp_gt_u32_e64 s[16:17], s16, v0
	s_add_u32 s30, s26, 0x3b500000
	v_cmp_eq_u32_e32 vcc, s58, v1
	s_addc_u32 s31, s27, 0
	s_and_b64 s[34:35], s[16:17], vcc
	s_add_u32 s59, s26, 0x50600008
	s_addc_u32 s60, s27, 0
	s_add_u32 s38, s26, 0x50500000
	s_addc_u32 s39, s27, 0
	s_and_b64 s[20:21], s[36:37], exec
	s_cselect_b32 s44, 0, 5
	s_mul_i32 s20, s43, 0x900
	v_mul_u32_u24_e32 v48, 0x110, v40
	v_lshrrev_b32_e32 v40, 4, v43
	s_add_i32 s20, s20, 0
	s_lshl_b32 s48, s43, 6
	s_mul_i32 s62, s44, 0x1100
	v_mul_u32_u24_e32 v49, 0x110, v40
	v_lshrrev_b32_e32 v40, 4, v41
	v_mov_b32_e32 v79, 0
	v_lshrrev_b32_e32 v1, 2, v0
	s_add_i32 s46, s20, 0x17200
	s_add_i32 s47, s56, 0
	s_add_i32 s49, s22, s48
	s_add_i32 s63, s62, 0x1100
	v_mul_u32_u24_e32 v50, 0x110, v40
	v_lshl_add_u64 v[40:41], s[26:27], 0, v[78:79]
	s_mov_b64 s[18:19], 0x55000000
	v_and_b32_e32 v84, 15, v0
	v_and_b32_e32 v132, 12, v1
	s_cmp_eq_u32 s44, 5
	v_lshl_add_u64 v[82:83], v[40:41], 0, s[18:19]
	v_mul_u32_u24_e32 v41, 0x110, v84
	v_and_b32_e32 v43, 48, v0
	v_cmp_eq_u32_e32 vcc, 0, v84
	s_cselect_b64 s[20:21], -1, 0
	v_lshl_or_b32 v141, s43, 4, v132
	v_add3_u32 v133, 0, v41, v43
	s_and_b64 s[40:41], vcc, s[20:21]
	s_add_i32 s20, 0, 0x19900
	v_add3_u32 v138, s47, v41, v43
	v_lshlrev_b32_e32 v41, 2, v141
	v_or_b32_e32 v145, 1, v141
	v_add_u32_e32 v142, s20, v41
	v_add_u32_e32 v143, s23, v41
	v_add_u32_e32 v144, s22, v41
	v_lshlrev_b32_e32 v41, 2, v145
	v_or_b32_e32 v149, 2, v141
	v_add_u32_e32 v146, s20, v41
	v_add_u32_e32 v147, s23, v41
	v_add_u32_e32 v148, s22, v41
	v_lshlrev_b32_e32 v41, 2, v149
	v_or_b32_e32 v154, 3, v141
	s_add_i32 s48, s48, s20
	v_add_u32_e32 v150, s20, v41
	v_add_u32_e32 v151, s23, v41
	v_add_u32_e32 v152, s22, v41
	v_lshlrev_b32_e32 v41, 2, v154
	s_add_u32 s64, s26, 0x5e100000
	v_add_u32_e32 v155, s20, v41
	v_add_u32_e32 v156, s23, v41
	v_add_u32_e32 v157, s22, v41
	v_bfe_u32 v41, v0, 4, 2
	s_movk_i32 s42, 0x110
	v_mul_u32_u24_e32 v45, 0x110, v218
	v_mul_u32_u24_e32 v47, 0x110, v85
	s_movk_i32 s14, 0x300
	v_lshlrev_b32_e32 v40, 7, v218
	v_lshlrev_b32_e32 v42, 7, v85
	s_movk_i32 s18, 0x210
	v_mul_u32_u24_e32 v51, 0x90, v84
	v_lshlrev_b32_e32 v52, 7, v84
	s_addc_u32 s65, s27, 0
	s_lshl_b32 s21, s44, 4
	v_lshlrev_b32_e32 v158, 4, v41
	v_mul_u32_u24_e32 v41, 0x240, v41
	v_cmp_gt_u32_e64 s[8:9], 16, v164
	v_cmp_gt_u32_e64 s[10:11], 32, v164
	v_cmp_gt_u32_e64 s[12:13], 48, v164
	s_mov_b32 s24, 0
	v_or_b32_e32 v117, 24, v100
	v_or_b32_e32 v120, 32, v100
	v_or_b32_e32 v123, 40, v100
	v_or_b32_e32 v126, 48, v100
	v_or_b32_e32 v129, 56, v100
	v_cmp_gt_u32_e64 s[14:15], s14, v0
	v_lshl_add_u64 v[80:81], s[30:31], 0, v[78:79]
	v_cmp_gt_u32_e64 s[18:19], s18, v0
	s_mul_i32 s61, s44, 0x900
	v_add_u32_e32 v134, s48, v164
	v_or_b32_e32 v1, 0x200, v0
	v_lshl_add_u32 v135, v164, 1, 0
	v_add3_u32 v136, s46, v51, v43
	v_sub_u32_e32 v137, v133, v52
	v_add_u32_e32 v139, 0xd900, v133
	v_lshl_add_u32 v140, v132, 2, s49
	v_mad_u32_u24 v159, v84, s42, v158
	v_lshl_or_b32 v160, v84, 1, v41
	v_mov_b32_e32 v161, 0xff61b1e6
	v_add_u32_e32 v162, v39, v45
	v_add_u32_e32 v163, v39, v47
	v_add_u32_e32 v168, v39, v48
	v_add_u32_e32 v169, v39, v49
	v_add_u32_e32 v170, v39, v50
	s_movk_i32 s66, 0x2e00
	v_lshlrev_b32_e32 v86, 1, v38
	v_lshlrev_b32_e32 v88, 1, v40
	v_lshlrev_b32_e32 v90, 1, v42
	v_lshlrev_b32_e32 v92, 1, v44
	v_lshlrev_b32_e32 v94, 1, v46
	s_mov_b32 s42, 0x3db504f3
	s_lshl_b32 s44, s21, 1
	v_mov_b32_e32 v171, 0x3f80
	v_mov_b32_e32 v172, 0x8100
	s_waitcnt vmcnt(0)
	s_branch .LBB0_3228

.LBB0_3228:
	s_ashr_i32 s20, s45, 31
	s_lshr_b32 s20, s20, 27
	s_add_i32 s20, s45, s20
	s_ashr_i32 s67, s20, 5
	s_and_b32 s68, s67, 1
	s_cmp_eq_u32 s68, 0
	s_cselect_b64 s[20:21], -1, 0
	s_cmp_eq_u32 s68, 1
	v_cndmask_b32_e64 v38, 0, 1, s[28:29]
	s_cselect_b64 s[46:47], -1, 0
	s_waitcnt vmcnt(12)
	v_mov_b32_e32 v78, v186
	v_cmp_ne_u32_e64 s[22:23], 1, v38
	s_andn2_b64 vcc, exec, s[28:29]
	s_cbranch_vccnz .LBB0_3234
	s_nop 0
	v_add_f32_dpp v38, v87, v87 row_shr:1 row_mask:0xf bank_mask:0xf bound_ctrl:1
	s_and_b64 vcc, exec, s[46:47]
	s_nop 0
	v_add_f32_dpp v38, v38, v38 row_shr:2 row_mask:0xf bank_mask:0xf bound_ctrl:1
	s_nop 1
	v_add_f32_dpp v38, v38, v38 row_shr:4 row_mask:0xf bank_mask:0xf bound_ctrl:1
	s_nop 1
	v_add_f32_dpp v38, v38, v38 row_shr:8 row_mask:0xf bank_mask:0xf bound_ctrl:1
	s_nop 0
	v_readlane_b32 s48, v38, 15
	v_readlane_b32 s49, v38, 31
	v_readlane_b32 s50, v38, 47
	v_mov_b32_e32 v39, s48
	v_cndmask_b32_e64 v39, 0, v39, s[0:1]
	v_add_f32_e32 v38, v38, v39
	v_mov_b32_e32 v39, s49
	v_cndmask_b32_e64 v39, 0, v39, s[4:5]
	v_add_f32_e32 v38, v38, v39
	v_mov_b32_e32 v39, s50
	v_cndmask_b32_e64 v39, 0, v39, s[6:7]
	v_add_f32_e32 v38, v38, v39
	s_nop 0
	v_readlane_b32 s48, v38, 63
	s_nop 1
	v_sub_f32_e32 v39, s48, v38
	v_add_f32_e32 v39, v87, v39
	v_cndmask_b32_e64 v38, v39, v38, s[20:21]
	v_sub_f32_e32 v39, v89, v38
	s_mov_b64 s[48:49], -1
	v_max_f32_e32 v40, v39, v39
	s_cbranch_vccz .LBB0_3231
	v_mov_b32_e32 v41, 0xff61b1e6
	v_mov_b32_e32 v42, 0xff61b1e6
	s_nop 0
	v_mov_b32_dpp v41, v39 row_shl:1 row_mask:0xf bank_mask:0xf
	v_max_f32_e32 v41, v41, v41
	v_max_f32_e32 v41, v40, v41
	s_nop 1
	v_mov_b32_dpp v42, v41 row_shl:2 row_mask:0xf bank_mask:0xf
	v_max_f32_e32 v42, v42, v42
	v_max_f32_e32 v41, v41, v42
	v_mov_b32_e32 v42, 0xff61b1e6
	s_nop 1
	v_mov_b32_dpp v42, v41 row_shl:4 row_mask:0xf bank_mask:0xf
	v_max_f32_e32 v42, v42, v42
	v_max_f32_e32 v41, v41, v42
	v_mov_b32_e32 v42, 0xff61b1e6
	s_nop 1
	v_mov_b32_dpp v42, v41 row_shl:8 row_mask:0xf bank_mask:0xf
	v_max_f32_e32 v42, v42, v42
	v_max_f32_e32 v41, v41, v42
	s_nop 0
	v_readlane_b32 s47, v41, 32
	v_readlane_b32 s48, v41, 48
	v_readlane_b32 s46, v41, 16
	v_max_f32_e64 v42, s47, s47
	v_max_f32_e64 v43, s48, s48
	v_mov_b32_e32 v44, s48
	v_max_f32_e32 v42, v43, v42
	v_max_f32_e64 v43, s46, s46
	v_cndmask_b32_e64 v44, v161, v44, s[12:13]
	v_max_f32_e32 v43, v42, v43
	v_cndmask_b32_e64 v42, v44, v42, s[10:11]
	v_cndmask_b32_e64 v42, v42, v43, s[8:9]
	v_max_f32_e32 v42, v42, v42
	v_max_f32_e32 v41, v41, v42
	s_mov_b64 s[48:49], 0

.LBB0_3887:
	s_cmp_gt_i32 s60, 27
	s_cselect_b64 s[0:1], -1, 0
	s_cmp_lt_i32 s61, 28
	s_cselect_b64 s[4:5], -1, 0
	s_or_b64 s[0:1], s[0:1], s[4:5]
	v_readlane_b32 s64, v247, 54
	s_and_b64 vcc, exec, s[0:1]
	v_readlane_b32 s70, v247, 60
	v_readlane_b32 s71, v247, 61
	s_mov_b64 s[72:73], s[60:61]
	v_readlane_b32 s65, v247, 55
	v_readlane_b32 s66, v247, 56
	v_readlane_b32 s67, v247, 57
	v_readlane_b32 s68, v247, 58
	v_readlane_b32 s69, v247, 59
	s_cbranch_vccnz .LBB0_3968
	s_barrier
	s_and_saveexec_b64 s[0:1], s[90:91]
	s_cbranch_execz .LBB0_3890
	s_waitcnt vmcnt(15)
	v_mov_b32_e32 v1, 0x10000
	global_load_dword v248, v1, s[26:27] sc1
	global_load_dword v249, v1, s[26:27] offset:256 sc1
	global_load_dword v250, v1, s[26:27] offset:512 sc1
	global_load_dword v251, v1, s[26:27] offset:768 sc1
	global_load_dword v252, v1, s[26:27] offset:1024 sc1
	global_load_dword v253, v1, s[26:27] offset:1280 sc1
	global_load_dword v254, v1, s[26:27] offset:1536 sc1
	global_load_dword v255, v1, s[26:27] offset:1792 sc1
	s_waitcnt vmcnt(0)
	v_mov_b32_e32 v2, v248
	s_add_i32 s6, 0, 0x20040
	s_add_i32 s4, 0, 0x20000
	v_mov_b32_e32 v3, 0
	s_add_i32 s7, 0, 0x20080
	v_mov_b32_e32 v6, s6
	s_add_i32 s5, 0, 0x20020
	v_mov_b32_e32 v4, s4
	v_mov_b32_e32 v7, s7
	ds_write_b32 v6, v3
	ds_write_b32 v7, v3
	v_mov_b32_e32 v5, s5
	s_add_i32 s6, 0, 0x20044
	s_add_i32 s4, 0, 0x20004
	s_add_i32 s7, 0, 0x20084
	v_mov_b32_e32 v6, s6
	s_add_i32 s5, 0, 0x20024
	v_mov_b32_e32 v7, s7
	s_add_i32 s6, 0, 0x20048
	s_add_i32 s7, 0, 0x20088
	s_waitcnt vmcnt(0)
	v_add_u32_e32 v3, 0xff, v2
	ds_write_b32 v4, v2
	v_ashrrev_i32_e32 v2, 8, v3
	ds_write_b32 v5, v2
	v_mov_b32_e32 v3, v249
	v_mov_b32_e32 v4, s4
	v_mul_lo_u32 v8, v2, 56
	ds_write_b32 v6, v2
	ds_write_b32 v7, v8
	v_mov_b32_e32 v5, s5
	v_mov_b32_e32 v7, s6
	s_add_i32 s4, 0, 0x20008
	s_add_i32 s5, 0, 0x20028
	v_mov_b32_e32 v8, s7
	s_add_i32 s6, 0, 0x2004c
	s_add_i32 s7, 0, 0x2008c
	s_waitcnt vmcnt(0)
	v_add_u32_e32 v6, 0xff, v3
	ds_write_b32 v4, v3
	v_ashrrev_i32_e32 v3, 8, v6
	ds_write_b32 v5, v3
	v_mov_b32_e32 v4, v250
	v_add_u32_e32 v2, v3, v2
	v_mul_lo_u32 v3, v2, 56
	ds_write_b32 v7, v2
	ds_write_b32 v8, v3
	v_mov_b32_e32 v5, s4
	v_mov_b32_e32 v6, s5
	v_mov_b32_e32 v7, s6
	s_add_i32 s4, 0, 0x2000c
	s_add_i32 s5, 0, 0x2002c
	v_mov_b32_e32 v8, s7
	s_add_i32 s6, 0, 0x20050
	s_add_i32 s7, 0, 0x20090
	s_waitcnt vmcnt(0)
	v_add_u32_e32 v3, 0xff, v4
	v_ashrrev_i32_e32 v3, 8, v3
	ds_write_b32 v5, v4
	ds_write_b32 v6, v3
	v_mov_b32_e32 v4, v251
	v_add_u32_e32 v2, v3, v2
	v_mul_lo_u32 v3, v2, 56
	ds_write_b32 v7, v2
	ds_write_b32 v8, v3
	v_mov_b32_e32 v5, s4
	v_mov_b32_e32 v6, s5
	v_mov_b32_e32 v7, s6
	s_add_i32 s4, 0, 0x20010
	s_add_i32 s5, 0, 0x20030
	v_mov_b32_e32 v8, s7
	s_add_i32 s6, 0, 0x20054
	s_add_i32 s7, 0, 0x20094
	s_waitcnt vmcnt(0)
	v_add_u32_e32 v3, 0xff, v4
	v_ashrrev_i32_e32 v3, 8, v3
	ds_write_b32 v5, v4
	ds_write_b32 v6, v3
	v_mov_b32_e32 v4, v252
	v_add_u32_e32 v2, v3, v2
	v_mul_lo_u32 v3, v2, 56
	ds_write_b32 v7, v2
	ds_write_b32 v8, v3
	v_mov_b32_e32 v5, s4
	v_mov_b32_e32 v6, s5
	v_mov_b32_e32 v7, s6
	s_add_i32 s4, 0, 0x20014
	s_add_i32 s5, 0, 0x20034
	v_mov_b32_e32 v8, s7
	s_add_i32 s6, 0, 0x20058
	s_add_i32 s7, 0, 0x20098
	s_waitcnt vmcnt(0)
	v_add_u32_e32 v3, 0xff, v4
	v_ashrrev_i32_e32 v3, 8, v3
	ds_write_b32 v5, v4
	ds_write_b32 v6, v3
	v_mov_b32_e32 v4, v253
	v_add_u32_e32 v2, v3, v2
	v_mul_lo_u32 v3, v2, 56
	ds_write_b32 v7, v2
	ds_write_b32 v8, v3
	v_mov_b32_e32 v5, s4
	v_mov_b32_e32 v6, s5
	v_mov_b32_e32 v7, s6
	s_add_i32 s4, 0, 0x20018
	s_add_i32 s5, 0, 0x20038
	v_mov_b32_e32 v8, s7
	s_add_i32 s6, 0, 0x2005c
	s_add_i32 s7, 0, 0x2009c
	s_waitcnt vmcnt(0)
	v_add_u32_e32 v3, 0xff, v4
	v_ashrrev_i32_e32 v3, 8, v3
	ds_write_b32 v5, v4
	ds_write_b32 v6, v3
	v_mov_b32_e32 v4, v254
	v_add_u32_e32 v2, v3, v2
	v_mul_lo_u32 v3, v2, 56
	ds_write_b32 v7, v2
	ds_write_b32 v8, v3
	v_mov_b32_e32 v5, s4
	v_mov_b32_e32 v6, s5
	s_add_i32 s4, 0, 0x2001c
	s_add_i32 s5, 0, 0x2003c
	s_waitcnt vmcnt(0)
	v_add_u32_e32 v3, 0xff, v4
	v_ashrrev_i32_e32 v3, 8, v3
	ds_write_b32 v5, v4
	ds_write_b32 v6, v3
	v_mov_b32_e32 v1, v255
	v_mov_b32_e32 v4, s4
	v_mov_b32_e32 v5, s5
	v_add_u32_e32 v2, v3, v2
	v_mov_b32_e32 v6, s6
	v_mul_lo_u32 v3, v2, 56
	s_waitcnt vmcnt(0)
	v_add_u32_e32 v7, 0xff, v1
	ds_write_b32 v4, v1
	v_ashrrev_i32_e32 v1, 8, v7
	ds_write_b32 v5, v1
	v_add_u32_e32 v1, v1, v2
	v_mul_lo_u32 v4, v1, 56
	ds_write2_b32 v6, v2, v1 offset1:1
	v_mov_b32_e32 v1, s7
	ds_write2_b32 v1, v3, v4 offset1:1

.LBB0_3968:
	s_cmp_gt_i32 s72, 28
	s_cselect_b64 s[0:1], -1, 0
	s_cmp_lt_i32 s73, 29
	s_cselect_b64 s[4:5], -1, 0
	s_or_b64 s[0:1], s[0:1], s[4:5]
	s_and_b64 vcc, exec, s[0:1]
	s_cbranch_vccnz .LBB0_4084
	s_waitcnt vmcnt(0)
	s_barrier
	s_and_saveexec_b64 s[0:1], s[90:91]
	s_cbranch_execz .LBB0_3971
	v_mov_b32_e32 v1, 0x10000
	global_load_dword v248, v1, s[26:27] sc1
	global_load_dword v249, v1, s[26:27] offset:256 sc1
	global_load_dword v250, v1, s[26:27] offset:512 sc1
	global_load_dword v251, v1, s[26:27] offset:768 sc1
	global_load_dword v252, v1, s[26:27] offset:1024 sc1
	global_load_dword v253, v1, s[26:27] offset:1280 sc1
	global_load_dword v254, v1, s[26:27] offset:1536 sc1
	global_load_dword v255, v1, s[26:27] offset:1792 sc1
	s_waitcnt vmcnt(0)
	v_mov_b32_e32 v2, v248
	s_add_i32 s6, 0, 0x20040
	s_add_i32 s4, 0, 0x20000
	v_mov_b32_e32 v3, 0
	s_add_i32 s7, 0, 0x20080
	v_mov_b32_e32 v6, s6
	s_add_i32 s5, 0, 0x20020
	v_mov_b32_e32 v4, s4
	v_mov_b32_e32 v7, s7
	ds_write_b32 v6, v3
	ds_write_b32 v7, v3
	v_mov_b32_e32 v5, s5
	s_add_i32 s6, 0, 0x20044
	s_add_i32 s4, 0, 0x20004
	s_add_i32 s7, 0, 0x20084
	v_mov_b32_e32 v6, s6
	s_add_i32 s5, 0, 0x20024
	v_mov_b32_e32 v7, s7
	s_add_i32 s6, 0, 0x20048
	s_add_i32 s7, 0, 0x20088
	s_waitcnt vmcnt(0)
	v_add_u32_e32 v3, 0xff, v2
	ds_write_b32 v4, v2
	v_ashrrev_i32_e32 v2, 8, v3
	ds_write_b32 v5, v2
	v_mov_b32_e32 v3, v249
	v_mov_b32_e32 v4, s4
	v_lshlrev_b32_e32 v8, 3, v2
	ds_write_b32 v6, v2
	ds_write_b32 v7, v8
	v_mov_b32_e32 v5, s5
	v_mov_b32_e32 v7, s6
	s_add_i32 s4, 0, 0x20008
	s_add_i32 s5, 0, 0x20028
	v_mov_b32_e32 v8, s7
	s_add_i32 s6, 0, 0x2004c
	s_add_i32 s7, 0, 0x2008c
	s_waitcnt vmcnt(0)
	v_add_u32_e32 v6, 0xff, v3
	ds_write_b32 v4, v3
	v_ashrrev_i32_e32 v3, 8, v6
	ds_write_b32 v5, v3
	v_mov_b32_e32 v4, v250
	v_add_u32_e32 v2, v3, v2
	v_lshlrev_b32_e32 v3, 3, v2
	ds_write_b32 v7, v2
	ds_write_b32 v8, v3
	v_mov_b32_e32 v5, s4
	v_mov_b32_e32 v6, s5
	v_mov_b32_e32 v7, s6
	s_add_i32 s4, 0, 0x2000c
	s_add_i32 s5, 0, 0x2002c
	v_mov_b32_e32 v8, s7
	s_add_i32 s6, 0, 0x20050
	s_add_i32 s7, 0, 0x20090
	s_waitcnt vmcnt(0)
	v_add_u32_e32 v3, 0xff, v4
	v_ashrrev_i32_e32 v3, 8, v3
	ds_write_b32 v5, v4
	ds_write_b32 v6, v3
	v_mov_b32_e32 v4, v251
	v_add_u32_e32 v2, v3, v2
	v_lshlrev_b32_e32 v3, 3, v2
	ds_write_b32 v7, v2
	ds_write_b32 v8, v3
	v_mov_b32_e32 v5, s4
	v_mov_b32_e32 v6, s5
	v_mov_b32_e32 v7, s6
	s_add_i32 s4, 0, 0x20010
	s_add_i32 s5, 0, 0x20030
	v_mov_b32_e32 v8, s7
	s_add_i32 s6, 0, 0x20054
	s_add_i32 s7, 0, 0x20094
	s_waitcnt vmcnt(0)
	v_add_u32_e32 v3, 0xff, v4
	v_ashrrev_i32_e32 v3, 8, v3
	ds_write_b32 v5, v4
	ds_write_b32 v6, v3
	v_mov_b32_e32 v4, v252
	v_add_u32_e32 v2, v3, v2
	v_lshlrev_b32_e32 v3, 3, v2
	ds_write_b32 v7, v2
	ds_write_b32 v8, v3
	v_mov_b32_e32 v5, s4
	v_mov_b32_e32 v6, s5
	v_mov_b32_e32 v7, s6
	s_add_i32 s4, 0, 0x20014
	s_add_i32 s5, 0, 0x20034
	v_mov_b32_e32 v8, s7
	s_add_i32 s6, 0, 0x20058
	s_add_i32 s7, 0, 0x20098
	s_waitcnt vmcnt(0)
	v_add_u32_e32 v3, 0xff, v4
	v_ashrrev_i32_e32 v3, 8, v3
	ds_write_b32 v5, v4
	ds_write_b32 v6, v3
	v_mov_b32_e32 v4, v253
	v_add_u32_e32 v2, v3, v2
	v_lshlrev_b32_e32 v3, 3, v2
	ds_write_b32 v7, v2
	ds_write_b32 v8, v3
	v_mov_b32_e32 v5, s4
	v_mov_b32_e32 v6, s5
	v_mov_b32_e32 v7, s6
	s_add_i32 s4, 0, 0x20018
	s_add_i32 s5, 0, 0x20038
	v_mov_b32_e32 v8, s7
	s_add_i32 s6, 0, 0x2005c
	s_add_i32 s7, 0, 0x2009c
	s_waitcnt vmcnt(0)
	v_add_u32_e32 v3, 0xff, v4
	v_ashrrev_i32_e32 v3, 8, v3
	ds_write_b32 v5, v4
	ds_write_b32 v6, v3
	v_mov_b32_e32 v4, v254
	v_add_u32_e32 v2, v3, v2
	v_lshlrev_b32_e32 v3, 3, v2
	ds_write_b32 v7, v2
	ds_write_b32 v8, v3
	v_mov_b32_e32 v5, s4
	v_mov_b32_e32 v6, s5
	s_add_i32 s4, 0, 0x2001c
	s_add_i32 s5, 0, 0x2003c
	s_waitcnt vmcnt(0)
	v_add_u32_e32 v3, 0xff, v4
	v_ashrrev_i32_e32 v3, 8, v3
	ds_write_b32 v5, v4
	ds_write_b32 v6, v3
	v_mov_b32_e32 v1, v255
	v_mov_b32_e32 v4, s4
	v_mov_b32_e32 v5, s5
	v_add_u32_e32 v2, v3, v2
	v_mov_b32_e32 v6, s6
	v_lshlrev_b32_e32 v3, 3, v2
	s_waitcnt vmcnt(0)
	v_add_u32_e32 v7, 0xff, v1
	ds_write_b32 v4, v1
	v_ashrrev_i32_e32 v1, 8, v7
	ds_write_b32 v5, v1
	v_add_u32_e32 v1, v1, v2
	v_lshlrev_b32_e32 v4, 3, v1
	ds_write2_b32 v6, v2, v1 offset1:1
	v_mov_b32_e32 v1, s7
	ds_write2_b32 v1, v3, v4 offset1:1

.LBB0_4084:
	s_cmp_gt_i32 s72, 29
	s_cselect_b64 s[0:1], -1, 0
	s_cmp_lt_i32 s73, 30
	s_cselect_b64 s[4:5], -1, 0
	s_or_b64 s[0:1], s[0:1], s[4:5]
	s_and_b64 vcc, exec, s[0:1]
	s_cbranch_vccnz .LBB0_4160
	s_waitcnt vmcnt(0)
	s_barrier
	s_and_saveexec_b64 s[0:1], s[90:91]
	s_cbranch_execz .LBB0_4087
	v_mov_b32_e32 v1, 0x10000
	global_load_dword v248, v1, s[26:27] sc1
	global_load_dword v249, v1, s[26:27] offset:256 sc1
	global_load_dword v250, v1, s[26:27] offset:512 sc1
	global_load_dword v251, v1, s[26:27] offset:768 sc1
	global_load_dword v252, v1, s[26:27] offset:1024 sc1
	global_load_dword v253, v1, s[26:27] offset:1280 sc1
	global_load_dword v254, v1, s[26:27] offset:1536 sc1
	global_load_dword v255, v1, s[26:27] offset:1792 sc1
	s_waitcnt vmcnt(0)
	v_mov_b32_e32 v2, v248
	s_add_i32 s6, 0, 0x20040
	s_add_i32 s4, 0, 0x20000
	v_mov_b32_e32 v3, 0
	s_add_i32 s7, 0, 0x20080
	v_mov_b32_e32 v6, s6
	s_add_i32 s5, 0, 0x20020
	v_mov_b32_e32 v4, s4
	v_mov_b32_e32 v7, s7
	ds_write_b32 v6, v3
	ds_write_b32 v7, v3
	v_mov_b32_e32 v5, s5
	s_add_i32 s6, 0, 0x20044
	s_add_i32 s4, 0, 0x20004
	s_add_i32 s7, 0, 0x20084
	v_mov_b32_e32 v6, s6
	s_add_i32 s5, 0, 0x20024
	v_mov_b32_e32 v7, s7
	s_add_i32 s6, 0, 0x20048
	s_add_i32 s7, 0, 0x20088
	s_waitcnt vmcnt(0)
	v_add_u32_e32 v3, 0xff, v2
	ds_write_b32 v4, v2
	v_ashrrev_i32_e32 v2, 8, v3
	ds_write_b32 v5, v2
	v_mov_b32_e32 v3, v249
	v_mov_b32_e32 v4, s4
	v_lshlrev_b32_e32 v8, 3, v2
	ds_write_b32 v6, v2
	ds_write_b32 v7, v8
	v_mov_b32_e32 v5, s5
	v_mov_b32_e32 v7, s6
	s_add_i32 s4, 0, 0x20008
	s_add_i32 s5, 0, 0x20028
	v_mov_b32_e32 v8, s7
	s_add_i32 s6, 0, 0x2004c
	s_add_i32 s7, 0, 0x2008c
	s_waitcnt vmcnt(0)
	v_add_u32_e32 v6, 0xff, v3
	ds_write_b32 v4, v3
	v_ashrrev_i32_e32 v3, 8, v6
	ds_write_b32 v5, v3
	v_mov_b32_e32 v4, v250
	v_add_u32_e32 v2, v3, v2
	v_lshlrev_b32_e32 v3, 3, v2
	ds_write_b32 v7, v2
	ds_write_b32 v8, v3
	v_mov_b32_e32 v5, s4
	v_mov_b32_e32 v6, s5
	v_mov_b32_e32 v7, s6
	s_add_i32 s4, 0, 0x2000c
	s_add_i32 s5, 0, 0x2002c
	v_mov_b32_e32 v8, s7
	s_add_i32 s6, 0, 0x20050
	s_add_i32 s7, 0, 0x20090
	s_waitcnt vmcnt(0)
	v_add_u32_e32 v3, 0xff, v4
	v_ashrrev_i32_e32 v3, 8, v3
	ds_write_b32 v5, v4
	ds_write_b32 v6, v3
	v_mov_b32_e32 v4, v251
	v_add_u32_e32 v2, v3, v2
	v_lshlrev_b32_e32 v3, 3, v2
	ds_write_b32 v7, v2
	ds_write_b32 v8, v3
	v_mov_b32_e32 v5, s4
	v_mov_b32_e32 v6, s5
	v_mov_b32_e32 v7, s6
	s_add_i32 s4, 0, 0x20010
	s_add_i32 s5, 0, 0x20030
	v_mov_b32_e32 v8, s7
	s_add_i32 s6, 0, 0x20054
	s_add_i32 s7, 0, 0x20094
	s_waitcnt vmcnt(0)
	v_add_u32_e32 v3, 0xff, v4
	v_ashrrev_i32_e32 v3, 8, v3
	ds_write_b32 v5, v4
	ds_write_b32 v6, v3
	v_mov_b32_e32 v4, v252
	v_add_u32_e32 v2, v3, v2
	v_lshlrev_b32_e32 v3, 3, v2
	ds_write_b32 v7, v2
	ds_write_b32 v8, v3
	v_mov_b32_e32 v5, s4
	v_mov_b32_e32 v6, s5
	v_mov_b32_e32 v7, s6
	s_add_i32 s4, 0, 0x20014
	s_add_i32 s5, 0, 0x20034
	v_mov_b32_e32 v8, s7
	s_add_i32 s6, 0, 0x20058
	s_add_i32 s7, 0, 0x20098
	s_waitcnt vmcnt(0)
	v_add_u32_e32 v3, 0xff, v4
	v_ashrrev_i32_e32 v3, 8, v3
	ds_write_b32 v5, v4
	ds_write_b32 v6, v3
	v_mov_b32_e32 v4, v253
	v_add_u32_e32 v2, v3, v2
	v_lshlrev_b32_e32 v3, 3, v2
	ds_write_b32 v7, v2
	ds_write_b32 v8, v3
	v_mov_b32_e32 v5, s4
	v_mov_b32_e32 v6, s5
	v_mov_b32_e32 v7, s6
	s_add_i32 s4, 0, 0x20018
	s_add_i32 s5, 0, 0x20038
	v_mov_b32_e32 v8, s7
	s_add_i32 s6, 0, 0x2005c
	s_add_i32 s7, 0, 0x2009c
	s_waitcnt vmcnt(0)
	v_add_u32_e32 v3, 0xff, v4
	v_ashrrev_i32_e32 v3, 8, v3
	ds_write_b32 v5, v4
	ds_write_b32 v6, v3
	v_mov_b32_e32 v4, v254
	v_add_u32_e32 v2, v3, v2
	v_lshlrev_b32_e32 v3, 3, v2
	ds_write_b32 v7, v2
	ds_write_b32 v8, v3
	v_mov_b32_e32 v5, s4
	v_mov_b32_e32 v6, s5
	s_add_i32 s4, 0, 0x2001c
	s_add_i32 s5, 0, 0x2003c
	s_waitcnt vmcnt(0)
	v_add_u32_e32 v3, 0xff, v4
	v_ashrrev_i32_e32 v3, 8, v3
	ds_write_b32 v5, v4
	ds_write_b32 v6, v3
	v_mov_b32_e32 v1, v255
	v_mov_b32_e32 v4, s4
	v_mov_b32_e32 v5, s5
	v_add_u32_e32 v2, v3, v2
	v_mov_b32_e32 v6, s6
	v_lshlrev_b32_e32 v3, 3, v2
	s_waitcnt vmcnt(0)
	v_add_u32_e32 v7, 0xff, v1
	ds_write_b32 v4, v1
	v_ashrrev_i32_e32 v1, 8, v7
	ds_write_b32 v5, v1
	v_add_u32_e32 v1, v1, v2
	v_lshlrev_b32_e32 v4, 3, v1
	ds_write2_b32 v6, v2, v1 offset1:1
	v_mov_b32_e32 v1, s7
	ds_write2_b32 v1, v3, v4 offset1:1

.LBB0_4160:
	s_cmp_gt_i32 s72, 30
	s_cselect_b64 s[0:1], -1, 0
	s_cmp_lt_i32 s73, 31
	s_cselect_b64 s[4:5], -1, 0
	s_or_b64 s[0:1], s[0:1], s[4:5]
	s_and_b64 vcc, exec, s[0:1]
	s_cbranch_vccnz .LBB0_4167
	s_waitcnt vmcnt(0)
	s_barrier
	s_and_saveexec_b64 s[0:1], s[90:91]
	s_cbranch_execz .LBB0_4163
	v_mov_b32_e32 v0, 0x10000
	global_load_dword v248, v0, s[26:27] sc1
	global_load_dword v249, v0, s[26:27] offset:256 sc1
	global_load_dword v250, v0, s[26:27] offset:512 sc1
	global_load_dword v251, v0, s[26:27] offset:768 sc1
	global_load_dword v252, v0, s[26:27] offset:1024 sc1
	global_load_dword v253, v0, s[26:27] offset:1280 sc1
	global_load_dword v254, v0, s[26:27] offset:1536 sc1
	global_load_dword v255, v0, s[26:27] offset:1792 sc1
	s_waitcnt vmcnt(0)
	v_mov_b32_e32 v1, v248
	v_mov_b32_e32 v2, 0
	ds_write_b32 v2, v2 offset:64
	ds_write_b32 v2, v2 offset:128
	s_waitcnt vmcnt(0)
	v_add_u32_e32 v3, 0xff, v1
	ds_write_b32 v2, v1
	v_ashrrev_i32_e32 v1, 8, v3
	ds_write_b32 v2, v1 offset:32
	v_mov_b32_e32 v3, v249
	ds_write_b32 v2, v1 offset:68
	ds_write_b32 v2, v1 offset:132
	s_waitcnt vmcnt(0)
	v_add_u32_e32 v4, 0xff, v3
	ds_write_b32 v2, v3 offset:4
	v_ashrrev_i32_e32 v3, 8, v4
	ds_write_b32 v2, v3 offset:36
	v_mov_b32_e32 v4, v250
	v_add_u32_e32 v1, v3, v1
	ds_write_b32 v2, v1 offset:72
	ds_write_b32 v2, v1 offset:136
	s_waitcnt vmcnt(0)
	v_add_u32_e32 v3, 0xff, v4
	v_ashrrev_i32_e32 v3, 8, v3
	ds_write_b32 v2, v4 offset:8
	ds_write_b32 v2, v3 offset:40
	v_mov_b32_e32 v4, v251
	v_add_u32_e32 v1, v3, v1
	ds_write_b32 v2, v1 offset:76
	ds_write_b32 v2, v1 offset:140
	s_waitcnt vmcnt(0)
	v_add_u32_e32 v3, 0xff, v4
	v_ashrrev_i32_e32 v3, 8, v3
	ds_write_b32 v2, v4 offset:12
	ds_write_b32 v2, v3 offset:44
	v_mov_b32_e32 v4, v252
	v_add_u32_e32 v1, v3, v1
	ds_write_b32 v2, v1 offset:80
	ds_write_b32 v2, v1 offset:144
	s_waitcnt vmcnt(0)
	v_add_u32_e32 v3, 0xff, v4
	v_ashrrev_i32_e32 v3, 8, v3
	ds_write_b32 v2, v4 offset:16
	ds_write_b32 v2, v3 offset:48
	v_mov_b32_e32 v4, v253
	v_add_u32_e32 v1, v3, v1
	ds_write_b32 v2, v1 offset:84
	ds_write_b32 v2, v1 offset:148
	s_waitcnt vmcnt(0)
	v_add_u32_e32 v3, 0xff, v4
	v_ashrrev_i32_e32 v3, 8, v3
	ds_write_b32 v2, v4 offset:20
	ds_write_b32 v2, v3 offset:52
	v_mov_b32_e32 v4, v254
	v_add_u32_e32 v1, v3, v1
	ds_write_b32 v2, v1 offset:88
	ds_write_b32 v2, v1 offset:152
	s_waitcnt vmcnt(0)
	v_add_u32_e32 v3, 0xff, v4
	v_ashrrev_i32_e32 v3, 8, v3
	ds_write_b32 v2, v4 offset:24
	ds_write_b32 v2, v3 offset:56
	v_mov_b32_e32 v0, v255
	v_add_u32_e32 v1, v3, v1
	s_waitcnt vmcnt(0)
	v_add_u32_e32 v3, 0xff, v0
	ds_write_b32 v2, v0 offset:28
	v_ashrrev_i32_e32 v0, 8, v3
	ds_write_b32 v2, v0 offset:60
	v_add_u32_e32 v0, v0, v1
	ds_write2_b32 v2, v1, v0 offset0:23 offset1:24
	ds_write2_b32 v2, v1, v0 offset0:39 offset1:40
